# adds GEMM1 epilogue: bf16 P-tile stores use sc1 nt cache policy (streaming output, not re-read inside the phase)
# baseline (speedup 1.0000x reference)
.LBB0_194:
	v_lshl_add_u32 v152, s85, 8, v1
	s_lshl_b32 s40, s14, 8
	s_cmp_lt_i32 s14, 58
	s_mov_b64 s[42:43], -1
	v_or_b32_e32 v150, 16, v152
	v_or_b32_e32 v148, 32, v152
	v_or_b32_e32 v146, 48, v152
	s_cbranch_scc0 .LBB0_196
	s_ashr_i32 s41, s40, 31
	v_lshl_add_u64 v[160:161], s[40:41], 1, v[138:139]
	s_movk_i32 s9, 0x7400
	v_mad_i64_i32 v[162:163], s[42:43], v152, s9, v[160:161]
	v_cvt_pk_bf16_f32 v156, v128, v129
	v_cvt_pk_bf16_f32 v157, v130, v131
	v_cvt_pk_bf16_f32 v158, v124, v125
	v_cvt_pk_bf16_f32 v159, v126, v127
	global_store_dwordx4 v[162:163], v[156:159], off sc1 nt
	v_add_u32_e32 v147, 0x80, v152
	s_nop 0
	v_cvt_pk_bf16_f32 v156, v108, v109
	v_cvt_pk_bf16_f32 v157, v110, v111
	v_cvt_pk_bf16_f32 v158, v100, v101
	v_cvt_pk_bf16_f32 v159, v102, v103
	global_store_dwordx4 v[162:163], v[156:159], off offset:256 sc1 nt
	v_mad_i64_i32 v[162:163], s[42:43], v150, s9, v[160:161]
	s_nop 0
	v_cvt_pk_bf16_f32 v156, v120, v121
	v_cvt_pk_bf16_f32 v157, v122, v123
	v_cvt_pk_bf16_f32 v158, v116, v117
	v_cvt_pk_bf16_f32 v159, v118, v119
	global_store_dwordx4 v[162:163], v[156:159], off sc1 nt
	s_nop 1
	v_cvt_pk_bf16_f32 v156, v92, v93
	v_cvt_pk_bf16_f32 v157, v94, v95
	v_cvt_pk_bf16_f32 v158, v84, v85
	v_cvt_pk_bf16_f32 v159, v86, v87
	global_store_dwordx4 v[162:163], v[156:159], off offset:256 sc1 nt
	v_mad_i64_i32 v[162:163], s[42:43], v148, s9, v[160:161]
	s_nop 0
	v_cvt_pk_bf16_f32 v156, v112, v113
	v_cvt_pk_bf16_f32 v157, v114, v115
	v_cvt_pk_bf16_f32 v158, v104, v105
	v_cvt_pk_bf16_f32 v159, v106, v107
	global_store_dwordx4 v[162:163], v[156:159], off sc1 nt
	s_nop 1
	v_cvt_pk_bf16_f32 v156, v80, v81
	v_cvt_pk_bf16_f32 v157, v82, v83
	v_cvt_pk_bf16_f32 v158, v76, v77
	v_cvt_pk_bf16_f32 v159, v78, v79
	global_store_dwordx4 v[162:163], v[156:159], off offset:256 sc1 nt
	v_mad_i64_i32 v[162:163], s[42:43], v146, s9, v[160:161]
	s_nop 0
	v_cvt_pk_bf16_f32 v156, v96, v97
	v_cvt_pk_bf16_f32 v157, v98, v99
	v_cvt_pk_bf16_f32 v158, v88, v89
	v_cvt_pk_bf16_f32 v159, v90, v91
	global_store_dwordx4 v[162:163], v[156:159], off sc1 nt
	s_nop 1
	v_cvt_pk_bf16_f32 v156, v72, v73
	v_cvt_pk_bf16_f32 v157, v74, v75
	v_cvt_pk_bf16_f32 v158, v68, v69
	v_cvt_pk_bf16_f32 v159, v70, v71
	global_store_dwordx4 v[162:163], v[156:159], off offset:256 sc1 nt
	v_mad_i64_i32 v[162:163], s[42:43], v147, s9, v[160:161]
	s_nop 0
	v_cvt_pk_bf16_f32 v156, v64, v65
	v_cvt_pk_bf16_f32 v157, v66, v67
	v_cvt_pk_bf16_f32 v158, v60, v61
	v_cvt_pk_bf16_f32 v159, v62, v63
	global_store_dwordx4 v[162:163], v[156:159], off sc1 nt
	v_add_u32_e32 v147, 0x90, v152
	s_nop 0
	v_cvt_pk_bf16_f32 v156, v48, v49
	v_cvt_pk_bf16_f32 v157, v50, v51
	v_cvt_pk_bf16_f32 v158, v44, v45
	v_cvt_pk_bf16_f32 v159, v46, v47
	global_store_dwordx4 v[162:163], v[156:159], off offset:256 sc1 nt
	v_mad_i64_i32 v[162:163], s[42:43], v147, s9, v[160:161]
	s_nop 0
	v_cvt_pk_bf16_f32 v156, v56, v57
	v_cvt_pk_bf16_f32 v157, v58, v59
	v_cvt_pk_bf16_f32 v158, v52, v53
	v_cvt_pk_bf16_f32 v159, v54, v55
	global_store_dwordx4 v[162:163], v[156:159], off sc1 nt
	v_add_u32_e32 v147, 0xa0, v152
	s_nop 0
	v_cvt_pk_bf16_f32 v156, v32, v33
	v_cvt_pk_bf16_f32 v157, v34, v35
	v_cvt_pk_bf16_f32 v158, v28, v29
	v_cvt_pk_bf16_f32 v159, v30, v31
	global_store_dwordx4 v[162:163], v[156:159], off offset:256 sc1 nt
	v_mad_i64_i32 v[162:163], s[42:43], v147, s9, v[160:161]
	s_nop 0
	v_cvt_pk_bf16_f32 v156, v40, v41
	v_cvt_pk_bf16_f32 v157, v42, v43
	v_cvt_pk_bf16_f32 v158, v36, v37
	v_cvt_pk_bf16_f32 v159, v38, v39
	global_store_dwordx4 v[162:163], v[156:159], off sc1 nt
	v_add_u32_e32 v147, 0xb0, v152
	v_mad_i64_i32 v[160:161], s[42:43], v147, s9, v[160:161]
	v_cvt_pk_bf16_f32 v156, v16, v17
	v_cvt_pk_bf16_f32 v157, v18, v19
	v_cvt_pk_bf16_f32 v158, v12, v13
	v_cvt_pk_bf16_f32 v159, v14, v15
	global_store_dwordx4 v[162:163], v[156:159], off offset:256 sc1 nt
	s_mov_b64 s[42:43], 0
	s_nop 0
	v_cvt_pk_bf16_f32 v156, v24, v25
	v_cvt_pk_bf16_f32 v157, v26, v27
	v_cvt_pk_bf16_f32 v158, v20, v21
	v_cvt_pk_bf16_f32 v159, v22, v23
	global_store_dwordx4 v[160:161], v[156:159], off sc1 nt
	s_nop 1
	v_cvt_pk_bf16_f32 v156, v8, v9
	v_cvt_pk_bf16_f32 v157, v10, v11
	v_cvt_pk_bf16_f32 v158, v4, v5
	v_cvt_pk_bf16_f32 v159, v6, v7
	global_store_dwordx4 v[160:161], v[156:159], off offset:256 sc1 nt
